# V tile by LDS-DMA in both attention phases; early transposed V reads for P.V d-tiles 4-7 in differential attention
# baseline (speedup 1.0000x reference)
; #define SBAR() __builtin_amdgcn_sched_barrier(0)
; #define MFMA16(a, b, c) __builtin_amdgcn_mfma_f32_16x16x32_bf16(a, b, c, 0, 0, 0)
; #define EWRITEK(b) do { char* d_ = K_lds + (b) * PB_K; *(bf16x8*)(d_ + KSWZ(sr, sc * 2)) = sk0; *(bf16x8*)(d_ + KSWZ(32 + sr, sc * 2)) = sk1; } while (0)
; template <int D0> __device__ __forceinline__ void pv16d(f32x4a (&o)[8][2], int vbo, int vbp, const bf16x8 (&po)[2], const bf16x8 (&pp)[2]) {
;     ...
;   const s16x4 a0 = TRO(D0, 0), a1 = TRO(D0, 1), a2 = TRP(D0, 0), a3 = TRP(D0, 1), b0 = TRO(D0 + 1, 0), b1 = TRO(D0 + 1, 1), b2 = TRP(D0 + 1, 0), b3 = TRP(D0 + 1, 1);
;   const s16x4 c0 = TRO(D0 + 2, 0), c1 = TRO(D0 + 2, 1), c2 = TRP(D0 + 2, 0), c3 = TRP(D0 + 2, 1);
;   asm volatile("s_waitcnt lgkmcnt(4)" ::: "memory"); SBAR();
;   o[D0][0] = MFMA16(PK16(a0, a1), po[0], o[D0][0]); o[D0][1] = MFMA16(PK16(a0, a1), po[1], o[D0][1]);
;   o[D0 + 1][0] = MFMA16(PK16(b0, b1), po[0], o[D0 + 1][0]); o[D0 + 1][1] = MFMA16(PK16(b0, b1), po[1], o[D0 + 1][1]);
;   o[D0][0] = MFMA16(PK16(a2, a3), pp[0], o[D0][0]); o[D0][1] = MFMA16(PK16(a2, a3), pp[1], o[D0][1]);
;   o[D0 + 1][0] = MFMA16(PK16(b2, b3), pp[0], o[D0 + 1][0]); o[D0 + 1][1] = MFMA16(PK16(b2, b3), pp[1], o[D0 + 1][1]);
;   SBAR();
;   const s16x4 d0 = TRO(D0 + 3, 0), d1 = TRO(D0 + 3, 1), d2 = TRP(D0 + 3, 0), d3 = TRP(D0 + 3, 1);
;   asm volatile("s_waitcnt lgkmcnt(4)" ::: "memory"); SBAR();
;   o[D0 + 2][0] = MFMA16(PK16(c0, c1), po[0], o[D0 + 2][0]); o[D0 + 2][1] = MFMA16(PK16(c0, c1), po[1], o[D0 + 2][1]);
;   o[D0 + 2][0] = MFMA16(PK16(c2, c3), pp[0], o[D0 + 2][0]); o[D0 + 2][1] = MFMA16(PK16(c2, c3), pp[1], o[D0 + 2][1]);
;   asm volatile("s_waitcnt lgkmcnt(0)" ::: "memory"); SBAR();
; template <int LDQ, int LDK, int LDV, int LDO, int DMX> ...
;     ...
;   for (int t = 0; t < NT; ++t) {
;     __syncthreads();
;     bf16x8 pp[2]; { const char* d_ = P_oth + (t & 1) * (4 * PB_P); pp[0] = *(const bf16x8*)(d_); pp[1] = *(const bf16x8*)(d_ + 1024); }
;     const bf16x8 pc[2] = {po[0], po[1]};
;     const bool more = t + 1 < NT;
;     if (more) EQK((t + 1) & 1);
;     const int vb = vlane + (t & 1) * (int)D16_V, vbo = vb + ch * 1024, vbp = vb + (1 - ch) * 1024;
;     SBAR(); pv16d<0>(o, vbo, vbp, pc, pp); SBAR();
;     asm volatile("s_waitcnt vmcnt(0)" ::: "memory");
;     if (t + 2 < NT) EWRITEK(t & 1);
.LBB0_1271:
	s_add_i32 s60, s55, -1
	s_and_b32 s57, s60, 1
	s_bitcmp1_b32 s55, 0
	s_cselect_b64 s[22:23], -1, 0
	s_and_b64 s[58:59], s[22:23], exec
	s_cselect_b32 s58, 0x4400, 0
	s_cselect_b32 s85, 0x8200, 0
	s_add_i32 s85, s85, s84
	v_add_u32_e32 v178, s58, v193
	s_waitcnt vmcnt(2) lgkmcnt(0)
	s_barrier
	ds_read_b128 v[132:135], v178
	ds_read_b128 v[136:139], v178 offset:64
	ds_read_b128 v[144:147], v178 offset:4352
	ds_read_b128 v[148:151], v178 offset:4416
	s_mov_b32 m0, s85
	s_nop 0
	global_load_lds_dwordx4 v253, s[74:75]
	s_add_i32 m0, s85, 0x800
	s_nop 0
	global_load_lds_dwordx4 v253, s[74:75] offset:32
	s_add_i32 m0, s85, 0x400
	s_nop 0
	global_load_lds_dwordx4 v253, s[76:77]
	s_add_i32 m0, s85, 0xc00
	s_nop 0
	global_load_lds_dwordx4 v253, s[76:77] offset:32
	s_add_u32 s74, s74, 0xc0000
	s_addc_u32 s75, s75, 0
	s_add_u32 s76, s76, 0xc0000
	s_addc_u32 s77, s77, 0
	s_waitcnt lgkmcnt(3)
	v_mfma_f32_16x16x32_bf16 v[140:143], v[132:135], v[4:7], 0
	s_mul_i32 s58, s57, 0x8200
	v_mfma_f32_16x16x32_bf16 v[132:135], v[132:135], v[20:23], 0
	s_waitcnt lgkmcnt(1)
	v_mfma_f32_16x16x32_bf16 v[152:155], v[144:147], v[4:7], 0
	v_mfma_f32_16x16x32_bf16 v[144:147], v[144:147], v[20:23], 0
	v_mfma_f32_16x16x32_bf16 v[140:143], v[136:139], v[8:11], v[140:143]
	v_mfma_f32_16x16x32_bf16 v[132:135], v[136:139], v[24:27], v[132:135]
	s_waitcnt lgkmcnt(0)
	v_mfma_f32_16x16x32_bf16 v[136:139], v[148:151], v[8:11], v[152:155]
	v_mfma_f32_16x16x32_bf16 v[144:147], v[148:151], v[24:27], v[144:147]
	ds_read_b128 v[148:151], v178 offset:128
	s_nop 0
	ds_read_b128 v[152:155], v178 offset:192
	s_waitcnt lgkmcnt(1)
	v_mfma_f32_16x16x32_bf16 v[140:143], v[148:151], v[12:15], v[140:143]
	v_mfma_f32_16x16x32_bf16 v[132:135], v[148:151], v[28:31], v[132:135]
	ds_read_b128 v[148:151], v178 offset:4480
	ds_read_b128 v[180:183], v178 offset:4544
	s_waitcnt lgkmcnt(1)
	v_mfma_f32_16x16x32_bf16 v[136:139], v[148:151], v[12:15], v[136:139]
	v_mfma_f32_16x16x32_bf16 v[204:207], v[148:151], v[28:31], v[144:147]
	v_mfma_f32_16x16x32_bf16 v[144:147], v[152:155], v[16:19], v[140:143]
	v_mfma_f32_16x16x32_bf16 v[140:143], v[152:155], v[32:35], v[132:135]
	s_nop 2
	v_lshl_add_u32 v132, s57, 14, v191
	ds_read_b128 v[148:151], v132
	ds_read_b128 v[152:155], v132 offset:1024
	v_add_u32_e32 v132, s58, v194
	s_waitcnt lgkmcnt(2)
	v_mfma_f32_16x16x32_bf16 v[136:139], v[180:183], v[16:19], v[136:139]
	v_add_u32_e32 v179, v132, v195
	v_add_u32_e32 v178, v132, v196
	v_mfma_f32_16x16x32_bf16 v[132:135], v[180:183], v[32:35], v[204:207]
	ds_read_b64_tr_b16 v[180:181], v179 offset:0
	ds_read_b64_tr_b16 v[182:183], v179 offset:0x200
	ds_read_b64_tr_b16 v[204:205], v178 offset:0
	ds_read_b64_tr_b16 v[206:207], v178 offset:0x200
	ds_read_b64_tr_b16 v[208:209], v179 offset:0x820
	ds_read_b64_tr_b16 v[210:211], v179 offset:0xa20
	ds_read_b64_tr_b16 v[212:213], v178 offset:0x820
	ds_read_b64_tr_b16 v[214:215], v178 offset:0xa20
	ds_read_b64_tr_b16 v[216:217], v179 offset:0x1040
	ds_read_b64_tr_b16 v[218:219], v179 offset:0x1240
	ds_read_b64_tr_b16 v[220:221], v178 offset:0x1040
	ds_read_b64_tr_b16 v[222:223], v178 offset:0x1240
	s_waitcnt lgkmcnt(4)
	s_nop 0
	v_mfma_f32_16x16x32_bf16 v[128:131], v[180:183], v[64:67], v[128:131]
	v_mfma_f32_16x16x32_bf16 v[124:127], v[180:183], v[68:71], v[124:127]
	v_mfma_f32_16x16x32_bf16 v[120:123], v[208:211], v[64:67], v[120:123]
	v_mfma_f32_16x16x32_bf16 v[112:115], v[208:211], v[68:71], v[112:115]
	s_waitcnt lgkmcnt(1)
	v_mfma_f32_16x16x32_bf16 v[128:131], v[204:207], v[148:151], v[128:131]
	s_waitcnt lgkmcnt(0)
	v_mfma_f32_16x16x32_bf16 v[124:127], v[204:207], v[152:155], v[124:127]
	v_mfma_f32_16x16x32_bf16 v[120:123], v[212:215], v[148:151], v[120:123]
	v_mfma_f32_16x16x32_bf16 v[112:115], v[212:215], v[152:155], v[112:115]
	ds_read_b64_tr_b16 v[180:181], v179 offset:0x1860
	ds_read_b64_tr_b16 v[182:183], v179 offset:0x1a60
	ds_read_b64_tr_b16 v[204:205], v178 offset:0x1860
	ds_read_b64_tr_b16 v[206:207], v178 offset:0x1a60
	s_waitcnt lgkmcnt(4)
	v_mfma_f32_16x16x32_bf16 v[108:111], v[216:219], v[64:67], v[108:111]
	s_waitcnt lgkmcnt(0)
	ds_read_b64_tr_b16 v[36:37], v179 offset:0x2080
	ds_read_b64_tr_b16 v[38:39], v179 offset:0x2280
	ds_read_b64_tr_b16 v[40:41], v178 offset:0x2080
	ds_read_b64_tr_b16 v[42:43], v178 offset:0x2280
	ds_read_b64_tr_b16 v[44:45], v179 offset:0x28a0
	ds_read_b64_tr_b16 v[46:47], v179 offset:0x2aa0
	ds_read_b64_tr_b16 v[48:49], v178 offset:0x28a0
	ds_read_b64_tr_b16 v[50:51], v178 offset:0x2aa0
	ds_read_b64_tr_b16 v[232:233], v179 offset:0x30c0
	ds_read_b64_tr_b16 v[234:235], v179 offset:0x32c0
	ds_read_b64_tr_b16 v[236:237], v178 offset:0x30c0
	ds_read_b64_tr_b16 v[238:239], v178 offset:0x32c0
	v_mfma_f32_16x16x32_bf16 v[116:119], v[216:219], v[68:71], v[116:119]
	v_mfma_f32_16x16x32_bf16 v[108:111], v[220:223], v[148:151], v[108:111]
	v_mfma_f32_16x16x32_bf16 v[116:119], v[220:223], v[152:155], v[116:119]
	v_mfma_f32_16x16x32_bf16 v[100:103], v[180:183], v[64:67], v[100:103]
	v_mfma_f32_16x16x32_bf16 v[104:107], v[180:183], v[68:71], v[104:107]
	v_mfma_f32_16x16x32_bf16 v[100:103], v[204:207], v[148:151], v[100:103]
	v_mfma_f32_16x16x32_bf16 v[104:107], v[204:207], v[152:155], v[104:107]
	s_waitcnt vmcnt(4)
	s_cmpk_gt_u32 s60, 0x101
	s_cbranch_scc1 .Lvd_kskip
	s_mulk_i32 s57, 0x4400
	v_add_u32_e32 v244, s57, v198
	s_nop 0
	ds_write_b128 v244, v[52:55]
	ds_write_b128 v244, v[56:59] offset:8704
; #define SBAR() __builtin_amdgcn_sched_barrier(0)
; #define MFMA16(a, b, c) __builtin_amdgcn_mfma_f32_16x16x32_bf16(a, b, c, 0, 0, 0)
; #define ELOADV(kt) do { const char* vb_ = (const char*)Vh + (size_t)(kt) * (64 * LDV * 2); sv0 = *(const bf16x8*)(vb_ + voff0); sv1 = *(const bf16x8*)(vb_ + voff1); sv2 = *(const bf16x8*)(vb_ + voff0 + 256); sv3 = *(const bf16x8*)(vb_ + voff1 + 256); } while (0)
; template <int D0> __device__ __forceinline__ void pv16d(f32x4a (&o)[8][2], int vbo, int vbp, const bf16x8 (&po)[2], const bf16x8 (&pp)[2]) {
;     ...
;   const s16x4 a0 = TRO(D0, 0), a1 = TRO(D0, 1), a2 = TRP(D0, 0), a3 = TRP(D0, 1), b0 = TRO(D0 + 1, 0), b1 = TRO(D0 + 1, 1), b2 = TRP(D0 + 1, 0), b3 = TRP(D0 + 1, 1);
;   const s16x4 c0 = TRO(D0 + 2, 0), c1 = TRO(D0 + 2, 1), c2 = TRP(D0 + 2, 0), c3 = TRP(D0 + 2, 1);
;   asm volatile("s_waitcnt lgkmcnt(4)" ::: "memory"); SBAR();
;   o[D0][0] = MFMA16(PK16(a0, a1), po[0], o[D0][0]); o[D0][1] = MFMA16(PK16(a0, a1), po[1], o[D0][1]);
;   o[D0 + 1][0] = MFMA16(PK16(b0, b1), po[0], o[D0 + 1][0]); o[D0 + 1][1] = MFMA16(PK16(b0, b1), po[1], o[D0 + 1][1]);
;   o[D0][0] = MFMA16(PK16(a2, a3), pp[0], o[D0][0]); o[D0][1] = MFMA16(PK16(a2, a3), pp[1], o[D0][1]);
;   o[D0 + 1][0] = MFMA16(PK16(b2, b3), pp[0], o[D0 + 1][0]); o[D0 + 1][1] = MFMA16(PK16(b2, b3), pp[1], o[D0 + 1][1]);
;   SBAR();
;   const s16x4 d0 = TRO(D0 + 3, 0), d1 = TRO(D0 + 3, 1), d2 = TRP(D0 + 3, 0), d3 = TRP(D0 + 3, 1);
;   asm volatile("s_waitcnt lgkmcnt(4)" ::: "memory"); SBAR();
;   o[D0 + 2][0] = MFMA16(PK16(c0, c1), po[0], o[D0 + 2][0]); o[D0 + 2][1] = MFMA16(PK16(c0, c1), po[1], o[D0 + 2][1]);
;   o[D0 + 2][0] = MFMA16(PK16(c2, c3), pp[0], o[D0 + 2][0]); o[D0 + 2][1] = MFMA16(PK16(c2, c3), pp[1], o[D0 + 2][1]);
;   asm volatile("s_waitcnt lgkmcnt(0)" ::: "memory"); SBAR();
;   o[D0 + 3][0] = MFMA16(PK16(d0, d1), po[0], o[D0 + 3][0]); o[D0 + 3][1] = MFMA16(PK16(d0, d1), po[1], o[D0 + 3][1]);
;   o[D0 + 3][0] = MFMA16(PK16(d2, d3), pp[0], o[D0 + 3][0]); o[D0 + 3][1] = MFMA16(PK16(d2, d3), pp[1], o[D0 + 3][1]);
;     ...
; }
; template <int LDQ, int LDK, int LDV, int LDO, int DMX> ...
;     ...
;     asm volatile("s_waitcnt vmcnt(0)" ::: "memory");
;     if (t + 2 < NT) EWRITEK(t & 1);
;     if (t + 1 < NT) EWRITEV((t + 1) & 1);
;     ELOADK(t + 3); ELOADV(t + 2);
;     SBAR(); pv16d<4>(o, vbo, vbp, pc, pp); SBAR();
;     if (more) ESM((t + 1) & 1);
;   }
.Lvd_kskip:
	v_lshl_add_u64 v[240:241], v[176:177], 0, s[6:7]
	v_add_co_u32_e32 v242, vcc, s41, v240
	s_nop 1
	v_addc_co_u32_e32 v243, vcc, 0, v241, vcc
	v_add_co_u32_e32 v240, vcc, s42, v240
	s_nop 1
	v_addc_co_u32_e32 v241, vcc, 0, v241, vcc
	global_load_dwordx4 v[52:55], v[242:243], off offset:1024
	global_load_dwordx4 v[56:59], v[240:241], off offset:1024
	s_waitcnt lgkmcnt(4)
	s_nop 0
	v_mfma_f32_16x16x32_bf16 v[84:87], v[36:39], v[64:67], v[84:87]
	v_mfma_f32_16x16x32_bf16 v[92:95], v[36:39], v[68:71], v[92:95]
	v_mfma_f32_16x16x32_bf16 v[88:91], v[44:47], v[64:67], v[88:91]
	v_mfma_f32_16x16x32_bf16 v[96:99], v[44:47], v[68:71], v[96:99]
	v_mfma_f32_16x16x32_bf16 v[84:87], v[40:43], v[148:151], v[84:87]
	v_mfma_f32_16x16x32_bf16 v[92:95], v[40:43], v[152:155], v[92:95]
	v_mfma_f32_16x16x32_bf16 v[88:91], v[48:51], v[148:151], v[88:91]
	v_mfma_f32_16x16x32_bf16 v[96:99], v[48:51], v[152:155], v[96:99]
	ds_read_b64_tr_b16 v[180:181], v179 offset:0x38e0
	ds_read_b64_tr_b16 v[182:183], v179 offset:0x3ae0
	ds_read_b64_tr_b16 v[204:205], v178 offset:0x38e0
	ds_read_b64_tr_b16 v[206:207], v178 offset:0x3ae0
	s_waitcnt lgkmcnt(4)
	v_mfma_f32_16x16x32_bf16 v[60:63], v[232:235], v[64:67], v[60:63]
	s_waitcnt lgkmcnt(0)
	v_mfma_f32_16x16x32_bf16 v[80:83], v[232:235], v[68:71], v[80:83]
	v_mfma_f32_16x16x32_bf16 v[60:63], v[236:239], v[148:151], v[60:63]
	v_mfma_f32_16x16x32_bf16 v[80:83], v[236:239], v[152:155], v[80:83]
	v_mfma_f32_16x16x32_bf16 v[64:67], v[180:183], v[64:67], v[72:75]
	v_mfma_f32_16x16x32_bf16 v[68:71], v[180:183], v[68:71], v[76:79]
	v_mfma_f32_16x16x32_bf16 v[72:75], v[204:207], v[148:151], v[64:67]
	v_mfma_f32_16x16x32_bf16 v[76:79], v[204:207], v[152:155], v[68:71]
	s_nop 4
	v_fmamk_f32 v64, v144, 0x3e0293ee, v200
	v_exp_f32_e32 v144, v64
	v_fmamk_f32 v64, v145, 0x3e0293ee, v200
	v_exp_f32_e32 v148, v64
	v_fmamk_f32 v64, v146, 0x3e0293ee, v200
	v_exp_f32_e32 v146, v64
	v_fmamk_f32 v64, v147, 0x3e0293ee, v200
	v_exp_f32_e32 v150, v64
	v_fmamk_f32 v64, v140, 0x3e0293ee, v200
	v_exp_f32_e32 v145, v64
	v_fmamk_f32 v64, v141, 0x3e0293ee, v200
	v_exp_f32_e32 v149, v64
	v_fmamk_f32 v64, v142, 0x3e0293ee, v200
	v_exp_f32_e32 v147, v64
	v_fmamk_f32 v64, v143, 0x3e0293ee, v200
	v_exp_f32_e32 v151, v64
	v_fmamk_f32 v64, v136, 0x3e0293ee, v200
	v_exp_f32_e32 v136, v64
	v_fmamk_f32 v64, v137, 0x3e0293ee, v200
	v_exp_f32_e32 v140, v64
	v_fmamk_f32 v64, v138, 0x3e0293ee, v200
	v_exp_f32_e32 v138, v64
	v_fmamk_f32 v64, v139, 0x3e0293ee, v200
	v_exp_f32_e32 v142, v64
	v_fmamk_f32 v64, v132, 0x3e0293ee, v200
	v_exp_f32_e32 v137, v64
	v_fmamk_f32 v64, v133, 0x3e0293ee, v200
	v_exp_f32_e32 v141, v64
	v_fmamk_f32 v64, v134, 0x3e0293ee, v200
	v_exp_f32_e32 v139, v64
	v_fmamk_f32 v64, v135, 0x3e0293ee, v200
	v_exp_f32_e32 v143, v64
	s_and_b32 s22, s56, 0x4000
	v_add_u32_e32 v132, s22, v190
	v_cvt_pk_bf16_f32 v64, v144, v148
	v_cvt_pk_bf16_f32 v65, v146, v150
	v_cvt_pk_bf16_f32 v66, v136, v140
	v_cvt_pk_bf16_f32 v67, v138, v142
	v_cvt_pk_bf16_f32 v68, v145, v149
	v_cvt_pk_bf16_f32 v69, v147, v151
	v_cvt_pk_bf16_f32 v70, v137, v141
	v_cvt_pk_bf16_f32 v71, v139, v143
	ds_write_b128 v132, v[64:67]
	ds_write_b128 v132, v[68:71] offset:1024
	v_pk_add_f32 v[132:133], v[144:145], v[148:149]
	v_pk_add_f32 v[134:135], v[146:147], v[150:151]
	s_add_u32 s6, s6, 0xc0000
	v_pk_add_f32 v[132:133], v[132:133], v[134:135]
	v_pk_add_f32 v[134:135], v[136:137], v[140:141]
	v_pk_add_f32 v[136:137], v[138:139], v[142:143]
	s_addc_u32 s7, s7, 0
	v_pk_add_f32 v[134:135], v[134:135], v[136:137]
	s_add_i32 s55, s55, 1
	v_pk_add_f32 v[132:133], v[132:133], v[134:135]
	s_addk_i32 s56, 0x4000
	s_cmp_eq_u32 s6, 0xc240000
	v_pk_add_f32 v[174:175], v[174:175], v[132:133]
	s_cbranch_scc0 .LBB0_1271
